# baseline (speedup 1.0000x reference)
_Z11init_kernelPKfS0_S0_S0_PDF16_S1_:
	s_load_dwordx8 s[4:11], s[0:1], 0x0
	s_load_dwordx4 s[12:15], s[0:1], 0x20
	v_readfirstlane_b32 s3, v0
	v_bfe_u32 v32, v0, 4, 2
	v_and_b32_e32 v33, 15, v0
	s_lshr_b32 s3, s3, 6
	s_lshl_b32 s17, s2, 11
	s_lshl_b32 s18, s2, 8
	s_lshl_b32 s19, s3, 7
	s_lshl_b32 s20, s3, 6
	v_mul_u32_u24_e32 v34, 36, v32
	v_lshl_or_b32 v34, v33, 7, v34
	v_mul_u32_u24_e32 v35, 0x900, v32
	v_lshl_or_b32 v35, v33, 3, v35
	v_lshlrev_b32_e32 v36, 3, v33
	v_lshlrev_b32_e32 v37, 4, v0
	v_lshlrev_b32_e32 v42, 9, v32
	v_lshl_or_b32 v42, v33, 2, v42
	v_mov_b32_e32 v44, 0
	v_mov_b32_e32 v45, 0
	v_mov_b32_e32 v46, 0
	v_mov_b32_e32 v47, 0
	v_mov_b32_e32 v39, 0
	v_mov_b32_e32 v41, 0
	v_add_u32_e32 v38, 20, v34
	v_lshlrev_b32_e32 v40, 4, v33
	v_cmp_eq_u32_e32 vcc, 3, v32
	s_waitcnt lgkmcnt(0)
	s_add_u32 s4, s4, s17
	s_addc_u32 s5, s5, 0
	s_add_u32 s6, s6, s18
	s_addc_u32 s7, s7, 0
	s_add_u32 s8, s8, s19
	s_addc_u32 s9, s9, 0
	v_lshl_add_u64 v[38:39], s[4:5], 0, v[38:39]
	v_lshl_add_u64 v[40:41], s[6:7], 0, v[40:41]
	v_cndmask_b32_e32 v38, v38, v40, vcc
	v_cndmask_b32_e32 v39, v39, v41, vcc
	global_load_dwordx4 v[2:5], v34, s[4:5] nt
	global_load_dword v6, v34, s[4:5] offset:16 nt
	global_load_dwordx4 v[8:11], v[38:39], off nt
	global_load_dwordx2 v[12:13], v35, s[8:9]
	global_load_dwordx2 v[14:15], v35, s[8:9] offset:256
	global_load_dwordx2 v[16:17], v35, s[8:9] offset:512
	global_load_dwordx2 v[18:19], v35, s[8:9] offset:768
	global_load_dwordx2 v[20:21], v35, s[8:9] offset:1024
	global_load_dwordx2 v[22:23], v35, s[8:9] offset:1280
	global_load_dwordx2 v[24:25], v35, s[8:9] offset:1536
	global_load_dwordx2 v[26:27], v35, s[8:9] offset:1792
	global_load_dwordx2 v[28:29], v35, s[8:9] offset:2048
	s_add_u32 s10, s10, s19
	s_addc_u32 s11, s11, 0
	global_load_dwordx2 v[30:31], v36, s[10:11]
	s_add_u32 s14, s14, s17
	s_addc_u32 s15, s15, 0
	s_add_u32 s12, s12, s17
	s_addc_u32 s13, s13, 0
	s_add_u32 s12, s12, s20
	s_addc_u32 s13, s13, 0
	global_store_dwordx4 v37, v[44:47], s[14:15] nt
	v_accvgpr_write_b32 a0, 0
	v_accvgpr_write_b32 a1, 0
	v_accvgpr_write_b32 a2, 0
	v_accvgpr_write_b32 a3, 0
	v_accvgpr_write_b32 a4, 0
	v_accvgpr_write_b32 a5, 0
	v_accvgpr_write_b32 a6, 0
	v_accvgpr_write_b32 a7, 0
	s_waitcnt vmcnt(11)
	s_waitcnt vmcnt(10)
	v_mfma_f32_16x16x4_f32 a[0:3], v2, v12, a[0:3]
	v_mfma_f32_16x16x4_f32 a[4:7], v2, v13, a[4:7]
	s_waitcnt vmcnt(9)
	v_mfma_f32_16x16x4_f32 a[0:3], v3, v14, a[0:3]
	v_mfma_f32_16x16x4_f32 a[4:7], v3, v15, a[4:7]
	s_waitcnt vmcnt(8)
	v_mfma_f32_16x16x4_f32 a[0:3], v4, v16, a[0:3]
	v_mfma_f32_16x16x4_f32 a[4:7], v4, v17, a[4:7]
	s_waitcnt vmcnt(7)
	v_mfma_f32_16x16x4_f32 a[0:3], v5, v18, a[0:3]
	v_mfma_f32_16x16x4_f32 a[4:7], v5, v19, a[4:7]
	s_waitcnt vmcnt(6)
	v_mfma_f32_16x16x4_f32 a[0:3], v6, v20, a[0:3]
	v_mfma_f32_16x16x4_f32 a[4:7], v6, v21, a[4:7]
	s_waitcnt vmcnt(5)
	v_mfma_f32_16x16x4_f32 a[0:3], v8, v22, a[0:3]
	v_mfma_f32_16x16x4_f32 a[4:7], v8, v23, a[4:7]
	s_waitcnt vmcnt(4)
	v_mfma_f32_16x16x4_f32 a[0:3], v9, v24, a[0:3]
	v_mfma_f32_16x16x4_f32 a[4:7], v9, v25, a[4:7]
	s_waitcnt vmcnt(3)
	v_mfma_f32_16x16x4_f32 a[0:3], v10, v26, a[0:3]
	v_mfma_f32_16x16x4_f32 a[4:7], v10, v27, a[4:7]
	s_waitcnt vmcnt(2)
	v_mfma_f32_16x16x4_f32 a[0:3], v11, v28, a[0:3]
	v_mfma_f32_16x16x4_f32 a[4:7], v11, v29, a[4:7]
	s_waitcnt vmcnt(1)
	s_nop 9
	v_accvgpr_read_b32 v2, a0
	v_accvgpr_read_b32 v3, a1
	v_accvgpr_read_b32 v4, a2
	v_accvgpr_read_b32 v5, a3
	v_accvgpr_read_b32 v6, a4
	v_accvgpr_read_b32 v7, a5
	v_accvgpr_read_b32 v8, a6
	v_accvgpr_read_b32 v9, a7
	v_add_f32_e32 v2, v30, v2
	v_add_f32_e32 v3, v30, v3
	v_add_f32_e32 v4, v30, v4
	v_add_f32_e32 v5, v30, v5
	v_add_f32_e32 v6, v31, v6
	v_add_f32_e32 v7, v31, v7
	v_add_f32_e32 v8, v31, v8
	v_add_f32_e32 v9, v31, v9
	v_cvt_pk_f16_f32 v2, v2, v6
	v_cvt_pk_f16_f32 v3, v3, v7
	v_cvt_pk_f16_f32 v4, v4, v8
	v_cvt_pk_f16_f32 v5, v5, v9
	global_store_dword v42, v2, s[12:13] nt
	global_store_dword v42, v3, s[12:13] offset:128 nt
	global_store_dword v42, v4, s[12:13] offset:256 nt
	global_store_dword v42, v5, s[12:13] offset:384 nt
	s_endpgm
	.p2align	8
